# out-proj EpiResid epilogue: 16 serialized residual load->wait->store steps replaced by two batches of 8 prefetched loads (dead MFMA fragment registers), same arithmetic
# speedup vs baseline: 1.0037x; 1.0037x over previous
.LBB0_1400:
	v_readlane_b32 s2, v252, 2
	v_readlane_b32 s3, v252, 3
	v_lshlrev_b64 v[172:173], 11, v[170:171]
	s_andn2_b64 vcc, exec, s[0:1]
	v_lshl_add_u64 v[172:173], s[2:3], 0, v[172:173]
	v_lshl_add_u64 v[172:173], v[168:169], 1, v[172:173]
	s_cbranch_vccnz .LBB0_1402
	v_mov_b32_e32 v242, v172
	v_mov_b32_e32 v243, v173
	v_mov_b32_e32 v244, v242
	v_mov_b32_e32 v245, v243
	s_mov_b64 s[0:1], 0x8000
	global_load_dwordx4 v[202:205], v[242:243], off
	global_load_dwordx4 v[206:209], v[242:243], off offset:256
	v_lshl_add_u64 v[242:243], v[242:243], 0, s[0:1]
	global_load_dwordx4 v[210:213], v[242:243], off
	global_load_dwordx4 v[214:217], v[242:243], off offset:256
	v_lshl_add_u64 v[242:243], v[242:243], 0, s[0:1]
	global_load_dwordx4 v[218:221], v[242:243], off
	global_load_dwordx4 v[222:225], v[242:243], off offset:256
	v_lshl_add_u64 v[242:243], v[242:243], 0, s[0:1]
	global_load_dwordx4 v[226:229], v[242:243], off
	global_load_dwordx4 v[230:233], v[242:243], off offset:256
	s_waitcnt vmcnt(0)
	v_lshlrev_b32_e32 v146, 16, v202
	v_and_b32_e32 v147, 0xffff0000, v202
	v_lshlrev_b32_e32 v148, 16, v203
	v_and_b32_e32 v149, 0xffff0000, v203
	v_lshlrev_b32_e32 v150, 16, v204
	v_and_b32_e32 v151, 0xffff0000, v204
	v_lshlrev_b32_e32 v152, 16, v205
	v_and_b32_e32 v153, 0xffff0000, v205
	v_fmac_f32_e32 v146, v142, v78
	v_fmac_f32_e32 v147, v143, v79
	v_fmac_f32_e32 v148, v144, v80
	v_fmac_f32_e32 v149, v145, v81
	v_fmac_f32_e32 v150, v138, v74
	v_fmac_f32_e32 v151, v139, v75
	v_fmac_f32_e32 v152, v140, v76
	v_fmac_f32_e32 v153, v141, v77
	v_cvt_pk_bf16_f32 v138, v146, v147
	v_cvt_pk_bf16_f32 v139, v148, v149
	v_cvt_pk_bf16_f32 v140, v150, v151
	v_cvt_pk_bf16_f32 v141, v152, v153
	global_store_dwordx4 v[244:245], v[138:141], off
	s_nop 1
	v_lshlrev_b32_e32 v138, 16, v206
	v_and_b32_e32 v139, 0xffff0000, v206
	v_lshlrev_b32_e32 v140, 16, v207
	v_and_b32_e32 v141, 0xffff0000, v207
	v_lshlrev_b32_e32 v142, 16, v208
	v_and_b32_e32 v143, 0xffff0000, v208
	v_lshlrev_b32_e32 v144, 16, v209
	v_and_b32_e32 v145, 0xffff0000, v209
	v_fmac_f32_e32 v138, v134, v62
	v_fmac_f32_e32 v139, v135, v63
	v_fmac_f32_e32 v142, v130, v58
	v_fmac_f32_e32 v140, v136, v64
	v_fmac_f32_e32 v141, v137, v65
	v_fmac_f32_e32 v143, v131, v59
	v_fmac_f32_e32 v144, v132, v60
	v_fmac_f32_e32 v145, v133, v61
	v_cvt_pk_bf16_f32 v130, v138, v139
	v_cvt_pk_bf16_f32 v131, v140, v141
	v_cvt_pk_bf16_f32 v132, v142, v143
	v_cvt_pk_bf16_f32 v133, v144, v145
	global_store_dwordx4 v[244:245], v[130:133], off offset:256
	s_nop 1
	v_lshl_add_u64 v[244:245], v[244:245], 0, s[0:1]
	v_lshlrev_b32_e32 v130, 16, v210
	v_and_b32_e32 v131, 0xffff0000, v210
	v_lshlrev_b32_e32 v132, 16, v211
	v_and_b32_e32 v133, 0xffff0000, v211
	v_lshlrev_b32_e32 v134, 16, v212
	v_and_b32_e32 v135, 0xffff0000, v212
	v_lshlrev_b32_e32 v136, 16, v213
	v_and_b32_e32 v137, 0xffff0000, v213
	v_fmac_f32_e32 v130, v126, v78
	v_fmac_f32_e32 v131, v127, v79
	v_fmac_f32_e32 v132, v128, v80
	v_fmac_f32_e32 v133, v129, v81
	v_fmac_f32_e32 v134, v122, v74
	v_fmac_f32_e32 v135, v123, v75
	v_fmac_f32_e32 v136, v124, v76
	v_fmac_f32_e32 v137, v125, v77
	v_cvt_pk_bf16_f32 v122, v130, v131
	v_cvt_pk_bf16_f32 v123, v132, v133
	v_cvt_pk_bf16_f32 v124, v134, v135
	v_cvt_pk_bf16_f32 v125, v136, v137
	global_store_dwordx4 v[244:245], v[122:125], off
	s_nop 1
	v_lshlrev_b32_e32 v122, 16, v214
	v_and_b32_e32 v123, 0xffff0000, v214
	v_lshlrev_b32_e32 v124, 16, v215
	v_and_b32_e32 v125, 0xffff0000, v215
	v_lshlrev_b32_e32 v126, 16, v216
	v_and_b32_e32 v127, 0xffff0000, v216
	v_lshlrev_b32_e32 v128, 16, v217
	v_and_b32_e32 v129, 0xffff0000, v217
	v_fmac_f32_e32 v122, v118, v62
	v_fmac_f32_e32 v123, v119, v63
	v_fmac_f32_e32 v126, v114, v58
	v_fmac_f32_e32 v124, v120, v64
	v_fmac_f32_e32 v125, v121, v65
	v_fmac_f32_e32 v127, v115, v59
	v_fmac_f32_e32 v128, v116, v60
	v_fmac_f32_e32 v129, v117, v61
	v_cvt_pk_bf16_f32 v114, v122, v123
	v_cvt_pk_bf16_f32 v115, v124, v125
	v_cvt_pk_bf16_f32 v116, v126, v127
	v_cvt_pk_bf16_f32 v117, v128, v129
	global_store_dwordx4 v[244:245], v[114:117], off offset:256
	s_nop 1
	v_lshl_add_u64 v[244:245], v[244:245], 0, s[0:1]
	v_lshlrev_b32_e32 v114, 16, v218
	v_and_b32_e32 v115, 0xffff0000, v218
	v_lshlrev_b32_e32 v116, 16, v219
	v_and_b32_e32 v117, 0xffff0000, v219
	v_lshlrev_b32_e32 v118, 16, v220
	v_and_b32_e32 v119, 0xffff0000, v220
	v_lshlrev_b32_e32 v120, 16, v221
	v_and_b32_e32 v121, 0xffff0000, v221
	v_fmac_f32_e32 v114, v110, v78
	v_fmac_f32_e32 v115, v111, v79
	v_fmac_f32_e32 v116, v112, v80
	v_fmac_f32_e32 v117, v113, v81
	v_fmac_f32_e32 v118, v106, v74
	v_fmac_f32_e32 v119, v107, v75
	v_fmac_f32_e32 v120, v108, v76
	v_fmac_f32_e32 v121, v109, v77
	v_cvt_pk_bf16_f32 v106, v114, v115
	v_cvt_pk_bf16_f32 v107, v116, v117
	v_cvt_pk_bf16_f32 v108, v118, v119
	v_cvt_pk_bf16_f32 v109, v120, v121
	global_store_dwordx4 v[244:245], v[106:109], off
	s_nop 1
	v_lshlrev_b32_e32 v106, 16, v222
	v_and_b32_e32 v107, 0xffff0000, v222
	v_lshlrev_b32_e32 v108, 16, v223
	v_and_b32_e32 v109, 0xffff0000, v223
	v_lshlrev_b32_e32 v110, 16, v224
	v_and_b32_e32 v111, 0xffff0000, v224
	v_lshlrev_b32_e32 v112, 16, v225
	v_and_b32_e32 v113, 0xffff0000, v225
	v_fmac_f32_e32 v106, v102, v62
	v_fmac_f32_e32 v107, v103, v63
	v_fmac_f32_e32 v110, v98, v58
	v_fmac_f32_e32 v108, v104, v64
	v_fmac_f32_e32 v109, v105, v65
	v_fmac_f32_e32 v111, v99, v59
	v_fmac_f32_e32 v112, v100, v60
	v_fmac_f32_e32 v113, v101, v61
	v_cvt_pk_bf16_f32 v98, v106, v107
	v_cvt_pk_bf16_f32 v99, v108, v109
	v_cvt_pk_bf16_f32 v100, v110, v111
	v_cvt_pk_bf16_f32 v101, v112, v113
	global_store_dwordx4 v[244:245], v[98:101], off offset:256
	s_nop 1
	v_lshl_add_u64 v[244:245], v[244:245], 0, s[0:1]
	v_lshlrev_b32_e32 v98, 16, v226
	v_and_b32_e32 v99, 0xffff0000, v226
	v_lshlrev_b32_e32 v100, 16, v227
	v_and_b32_e32 v101, 0xffff0000, v227
	v_lshlrev_b32_e32 v102, 16, v228
	v_and_b32_e32 v103, 0xffff0000, v228
	v_lshlrev_b32_e32 v104, 16, v229
	v_and_b32_e32 v105, 0xffff0000, v229
	v_fmac_f32_e32 v98, v94, v78
	v_fmac_f32_e32 v99, v95, v79
	v_fmac_f32_e32 v100, v96, v80
	v_fmac_f32_e32 v101, v97, v81
	v_fmac_f32_e32 v102, v90, v74
	v_fmac_f32_e32 v103, v91, v75
	v_fmac_f32_e32 v104, v92, v76
	v_fmac_f32_e32 v105, v93, v77
	v_cvt_pk_bf16_f32 v90, v98, v99
	v_cvt_pk_bf16_f32 v91, v100, v101
	v_cvt_pk_bf16_f32 v92, v102, v103
	v_cvt_pk_bf16_f32 v93, v104, v105
	global_store_dwordx4 v[244:245], v[90:93], off
	s_nop 1
	v_lshlrev_b32_e32 v90, 16, v230
	v_and_b32_e32 v91, 0xffff0000, v230
	v_lshlrev_b32_e32 v92, 16, v231
	v_and_b32_e32 v93, 0xffff0000, v231
	v_lshlrev_b32_e32 v94, 16, v232
	v_and_b32_e32 v95, 0xffff0000, v232
	v_lshlrev_b32_e32 v96, 16, v233
	v_and_b32_e32 v97, 0xffff0000, v233
	v_fmac_f32_e32 v90, v86, v62
	v_fmac_f32_e32 v91, v87, v63
	v_fmac_f32_e32 v94, v82, v58
	v_fmac_f32_e32 v92, v88, v64
	v_fmac_f32_e32 v93, v89, v65
	v_fmac_f32_e32 v95, v83, v59
	v_fmac_f32_e32 v96, v84, v60
	v_fmac_f32_e32 v97, v85, v61
	v_cvt_pk_bf16_f32 v82, v90, v91
	v_cvt_pk_bf16_f32 v83, v92, v93
	v_cvt_pk_bf16_f32 v84, v94, v95
	v_cvt_pk_bf16_f32 v85, v96, v97
	global_store_dwordx4 v[244:245], v[82:85], off offset:256
	s_nop 1
	s_mov_b64 s[0:1], 0x40000
	v_lshl_add_u64 v[242:243], v[172:173], 0, s[0:1]
	v_mov_b32_e32 v244, v242
	v_mov_b32_e32 v245, v243
	s_mov_b64 s[0:1], 0x8000
	global_load_dwordx4 v[202:205], v[242:243], off
	global_load_dwordx4 v[206:209], v[242:243], off offset:256
	v_lshl_add_u64 v[242:243], v[242:243], 0, s[0:1]
	global_load_dwordx4 v[210:213], v[242:243], off
	global_load_dwordx4 v[214:217], v[242:243], off offset:256
	v_lshl_add_u64 v[242:243], v[242:243], 0, s[0:1]
	global_load_dwordx4 v[218:221], v[242:243], off
	global_load_dwordx4 v[222:225], v[242:243], off offset:256
	v_lshl_add_u64 v[242:243], v[242:243], 0, s[0:1]
	global_load_dwordx4 v[226:229], v[242:243], off
	global_load_dwordx4 v[230:233], v[242:243], off offset:256
	s_waitcnt vmcnt(0)
	v_lshlrev_b32_e32 v82, 16, v202
	v_and_b32_e32 v83, 0xffff0000, v202
	v_lshlrev_b32_e32 v84, 16, v203
	v_and_b32_e32 v85, 0xffff0000, v203
	v_lshlrev_b32_e32 v86, 16, v204
	v_and_b32_e32 v87, 0xffff0000, v204
	v_lshlrev_b32_e32 v88, 16, v205
	v_and_b32_e32 v89, 0xffff0000, v205
	v_fmac_f32_e32 v82, v70, v78
	v_fmac_f32_e32 v83, v71, v79
	v_fmac_f32_e32 v84, v72, v80
	v_fmac_f32_e32 v85, v73, v81
	v_fmac_f32_e32 v86, v66, v74
	v_fmac_f32_e32 v87, v67, v75
	v_fmac_f32_e32 v88, v68, v76
	v_fmac_f32_e32 v89, v69, v77
	v_cvt_pk_bf16_f32 v66, v82, v83
	v_cvt_pk_bf16_f32 v67, v84, v85
	v_cvt_pk_bf16_f32 v68, v86, v87
	v_cvt_pk_bf16_f32 v69, v88, v89
	global_store_dwordx4 v[244:245], v[66:69], off
	s_nop 1
	v_lshlrev_b32_e32 v66, 16, v206
	v_and_b32_e32 v67, 0xffff0000, v206
	v_lshlrev_b32_e32 v68, 16, v207
	v_and_b32_e32 v69, 0xffff0000, v207
	v_lshlrev_b32_e32 v70, 16, v208
	v_and_b32_e32 v71, 0xffff0000, v208
	v_lshlrev_b32_e32 v72, 16, v209
	v_and_b32_e32 v73, 0xffff0000, v209
	v_fmac_f32_e32 v66, v54, v62
	v_fmac_f32_e32 v67, v55, v63
	v_fmac_f32_e32 v70, v50, v58
	v_fmac_f32_e32 v68, v56, v64
	v_fmac_f32_e32 v69, v57, v65
	v_fmac_f32_e32 v71, v51, v59
	v_fmac_f32_e32 v72, v52, v60
	v_fmac_f32_e32 v73, v53, v61
	v_cvt_pk_bf16_f32 v50, v66, v67
	v_cvt_pk_bf16_f32 v51, v68, v69
	v_cvt_pk_bf16_f32 v52, v70, v71
	v_cvt_pk_bf16_f32 v53, v72, v73
	global_store_dwordx4 v[244:245], v[50:53], off offset:256
	s_nop 1
	v_lshl_add_u64 v[244:245], v[244:245], 0, s[0:1]
	v_lshlrev_b32_e32 v50, 16, v210
	v_and_b32_e32 v51, 0xffff0000, v210
	v_lshlrev_b32_e32 v52, 16, v211
	v_and_b32_e32 v53, 0xffff0000, v211
	v_lshlrev_b32_e32 v54, 16, v212
	v_and_b32_e32 v55, 0xffff0000, v212
	v_lshlrev_b32_e32 v56, 16, v213
	v_and_b32_e32 v57, 0xffff0000, v213
	v_fmac_f32_e32 v50, v46, v78
	v_fmac_f32_e32 v51, v47, v79
	v_fmac_f32_e32 v52, v48, v80
	v_fmac_f32_e32 v53, v49, v81
	v_fmac_f32_e32 v54, v42, v74
	v_fmac_f32_e32 v55, v43, v75
	v_fmac_f32_e32 v56, v44, v76
	v_fmac_f32_e32 v57, v45, v77
	v_cvt_pk_bf16_f32 v42, v50, v51
	v_cvt_pk_bf16_f32 v43, v52, v53
	v_cvt_pk_bf16_f32 v44, v54, v55
	v_cvt_pk_bf16_f32 v45, v56, v57
	global_store_dwordx4 v[244:245], v[42:45], off
	s_nop 1
	v_lshlrev_b32_e32 v42, 16, v214
	v_and_b32_e32 v43, 0xffff0000, v214
	v_lshlrev_b32_e32 v44, 16, v215
	v_and_b32_e32 v45, 0xffff0000, v215
	v_lshlrev_b32_e32 v46, 16, v216
	v_and_b32_e32 v47, 0xffff0000, v216
	v_lshlrev_b32_e32 v48, 16, v217
	v_and_b32_e32 v49, 0xffff0000, v217
	v_fmac_f32_e32 v42, v38, v62
	v_fmac_f32_e32 v43, v39, v63
	v_fmac_f32_e32 v46, v34, v58
	v_fmac_f32_e32 v44, v40, v64
	v_fmac_f32_e32 v45, v41, v65
	v_fmac_f32_e32 v47, v35, v59
	v_fmac_f32_e32 v48, v36, v60
	v_fmac_f32_e32 v49, v37, v61
	v_cvt_pk_bf16_f32 v34, v42, v43
	v_cvt_pk_bf16_f32 v35, v44, v45
	v_cvt_pk_bf16_f32 v36, v46, v47
	v_cvt_pk_bf16_f32 v37, v48, v49
	global_store_dwordx4 v[244:245], v[34:37], off offset:256
	s_nop 1
	v_lshl_add_u64 v[244:245], v[244:245], 0, s[0:1]
	v_lshlrev_b32_e32 v34, 16, v218
	v_and_b32_e32 v35, 0xffff0000, v218
	v_lshlrev_b32_e32 v36, 16, v219
	v_and_b32_e32 v37, 0xffff0000, v219
	v_lshlrev_b32_e32 v38, 16, v220
	v_and_b32_e32 v39, 0xffff0000, v220
	v_lshlrev_b32_e32 v40, 16, v221
	v_and_b32_e32 v41, 0xffff0000, v221
	v_fmac_f32_e32 v34, v30, v78
	v_fmac_f32_e32 v35, v31, v79
	v_fmac_f32_e32 v36, v32, v80
	v_fmac_f32_e32 v37, v33, v81
	v_fmac_f32_e32 v38, v26, v74
	v_fmac_f32_e32 v39, v27, v75
	v_fmac_f32_e32 v40, v28, v76
	v_fmac_f32_e32 v41, v29, v77
	v_cvt_pk_bf16_f32 v26, v34, v35
	v_cvt_pk_bf16_f32 v27, v36, v37
	v_cvt_pk_bf16_f32 v28, v38, v39
	v_cvt_pk_bf16_f32 v29, v40, v41
	global_store_dwordx4 v[244:245], v[26:29], off
	s_nop 1
	v_lshlrev_b32_e32 v26, 16, v222
	v_and_b32_e32 v27, 0xffff0000, v222
	v_lshlrev_b32_e32 v28, 16, v223
	v_and_b32_e32 v29, 0xffff0000, v223
	v_lshlrev_b32_e32 v30, 16, v224
	v_and_b32_e32 v31, 0xffff0000, v224
	v_lshlrev_b32_e32 v32, 16, v225
	v_and_b32_e32 v33, 0xffff0000, v225
	v_fmac_f32_e32 v26, v22, v62
	v_fmac_f32_e32 v27, v23, v63
	v_fmac_f32_e32 v30, v18, v58
	v_fmac_f32_e32 v28, v24, v64
	v_fmac_f32_e32 v29, v25, v65
	v_fmac_f32_e32 v31, v19, v59
	v_fmac_f32_e32 v32, v20, v60
	v_fmac_f32_e32 v33, v21, v61
	v_cvt_pk_bf16_f32 v18, v26, v27
	v_cvt_pk_bf16_f32 v19, v28, v29
	v_cvt_pk_bf16_f32 v20, v30, v31
	v_cvt_pk_bf16_f32 v21, v32, v33
	global_store_dwordx4 v[244:245], v[18:21], off offset:256
	s_nop 1
	v_lshl_add_u64 v[244:245], v[244:245], 0, s[0:1]
	v_lshlrev_b32_e32 v18, 16, v226
	v_and_b32_e32 v19, 0xffff0000, v226
	v_lshlrev_b32_e32 v20, 16, v227
	v_and_b32_e32 v21, 0xffff0000, v227
	v_lshlrev_b32_e32 v22, 16, v228
	v_and_b32_e32 v23, 0xffff0000, v228
	v_lshlrev_b32_e32 v24, 16, v229
	v_and_b32_e32 v25, 0xffff0000, v229
	v_fmac_f32_e32 v18, v14, v78
	v_fmac_f32_e32 v19, v15, v79
	v_fmac_f32_e32 v20, v16, v80
	v_fmac_f32_e32 v21, v17, v81
	v_fmac_f32_e32 v22, v10, v74
	v_fmac_f32_e32 v23, v11, v75
	v_fmac_f32_e32 v24, v12, v76
	v_fmac_f32_e32 v25, v13, v77
	v_cvt_pk_bf16_f32 v10, v18, v19
	v_cvt_pk_bf16_f32 v11, v20, v21
	v_cvt_pk_bf16_f32 v12, v22, v23
	v_cvt_pk_bf16_f32 v13, v24, v25
	global_store_dwordx4 v[244:245], v[10:13], off
	s_nop 1
	v_lshlrev_b32_e32 v10, 16, v230
	v_and_b32_e32 v11, 0xffff0000, v230
	v_lshlrev_b32_e32 v12, 16, v231
	v_and_b32_e32 v13, 0xffff0000, v231
	v_lshlrev_b32_e32 v14, 16, v232
	v_and_b32_e32 v15, 0xffff0000, v232
	v_lshlrev_b32_e32 v16, 16, v233
	v_and_b32_e32 v17, 0xffff0000, v233
	v_fmac_f32_e32 v10, v6, v62
	v_fmac_f32_e32 v11, v7, v63
	v_fmac_f32_e32 v12, v8, v64
	v_fmac_f32_e32 v13, v9, v65
	v_fmac_f32_e32 v14, v2, v58
	v_fmac_f32_e32 v15, v3, v59
	v_fmac_f32_e32 v16, v4, v60
	v_fmac_f32_e32 v17, v5, v61
	v_cvt_pk_bf16_f32 v2, v10, v11
	v_cvt_pk_bf16_f32 v3, v12, v13
	v_cvt_pk_bf16_f32 v4, v14, v15
	v_cvt_pk_bf16_f32 v5, v16, v17
	global_store_dwordx4 v[244:245], v[2:5], off offset:256
	s_nop 1
	s_andn2_b64 vcc, exec, s[52:53]
	s_mov_b64 s[0:1], -1
	s_branch OPE_TAIL
	global_load_dwordx4 v[150:153], v[172:173], off
	s_waitcnt vmcnt(0)
	v_lshlrev_b32_e32 v146, 16, v150
	v_and_b32_e32 v147, 0xffff0000, v150
	v_lshlrev_b32_e32 v148, 16, v151
	v_and_b32_e32 v149, 0xffff0000, v151
	v_lshlrev_b32_e32 v150, 16, v152
	v_and_b32_e32 v151, 0xffff0000, v152
	v_lshlrev_b32_e32 v152, 16, v153
	v_and_b32_e32 v153, 0xffff0000, v153

OPE_TAIL:
	s_cbranch_vccnz .LBB0_1390
	s_andn2_b64 vcc, exec, s[6:7]
	s_cbranch_vccnz .LBB0_1389
	s_barrier
	s_branch .LBB0_1389
